# grid barrier acquire: L1 invalidate requested when thread 0 starts waiting (leader: with its release write-back) instead of after the generation flip (on top of v24)
# speedup vs baseline: 1.0090x; 1.0090x over previous
.LBB0_288:
	s_or_b64 exec, exec, s[14:15]
	v_cvt_f32_u32_e32 v6, v4
	s_waitcnt vmcnt(0)
	v_readfirstlane_b32 s14, v5
	v_sub_u32_e32 v5, 0, v4
	v_rcp_iflag_f32_e32 v6, v6
	v_add_u32_e32 v7, s14, v3
	v_mul_f32_e32 v6, 0x4f7ffffe, v6
	v_cvt_u32_f32_e32 v6, v6
	v_mul_lo_u32 v3, v5, v6
	v_mul_hi_u32 v3, v6, v3
	v_add_u32_e32 v3, v6, v3
	v_mul_hi_u32 v3, v7, v3
	v_mul_lo_u32 v5, v3, v4
	v_sub_u32_e32 v5, v7, v5
	v_add_u32_e32 v6, 1, v3
	v_cmp_ge_u32_e32 vcc, v5, v4
	s_nop 1
	v_cndmask_b32_e32 v3, v3, v6, vcc
	v_sub_u32_e32 v6, v5, v4
	v_cndmask_b32_e32 v5, v5, v6, vcc
	v_add_u32_e32 v6, 1, v3
	v_cmp_ge_u32_e32 vcc, v5, v4
	v_add_u32_e32 v5, 1, v7
	s_nop 0
	v_cndmask_b32_e32 v3, v3, v6, vcc
	v_mul_lo_u32 v6, v4, v3
	v_add_u32_e32 v4, v6, v4
	v_cmp_ne_u32_e32 vcc, v5, v4
	s_and_saveexec_b64 s[14:15], vcc
	s_xor_b64 s[30:31], exec, s[14:15]
	s_cbranch_execz .LBB0_302
	buffer_inv sc1
	v_readlane_b32 s14, v254, 41
	v_readlane_b32 s15, v254, 42
	s_waitcnt lgkmcnt(0)
	s_nop 3
	global_load_dword v2, v195, s[14:15] sc1
	s_waitcnt vmcnt(0)
	v_cmp_eq_u32_e32 vcc, v2, v3
	s_and_saveexec_b64 s[34:35], vcc
	s_cbranch_execz .LBB0_301
	s_mov_b32 s29, 1
	s_mov_b64 s[36:37], 0
	s_branch .LBB0_292

.LBB0_301:
	s_or_b64 exec, exec, s[34:35]
	s_waitcnt vmcnt(0)
	s_waitcnt vmcnt(0)
.LBB0_302:
	s_andn2_saveexec_b64 s[14:15], s[30:31]
	s_cbranch_execz .LBB0_322
	s_mov_b64 s[14:15], exec
	buffer_wbl2 sc1
	buffer_inv sc1
	s_waitcnt lgkmcnt(0)
	s_waitcnt vmcnt(0)
	v_mbcnt_lo_u32_b32 v3, s14, 0
	v_mbcnt_hi_u32_b32 v3, s15, v3
	v_cmp_eq_u32_e32 vcc, 0, v3
	s_and_saveexec_b64 s[30:31], vcc
	s_cbranch_execz .LBB0_305
	s_bcnt1_i32_b64 s14, s[14:15]
	v_mov_b32_e32 v4, s14
	v_readlane_b32 s14, v254, 43
	v_readlane_b32 s15, v254, 44
	s_nop 4
	global_atomic_add v4, v195, v4, s[14:15] sc0

.LBB0_319:
	s_or_b64 exec, exec, s[14:15]
	s_mov_b64 s[14:15], exec
	v_mbcnt_lo_u32_b32 v2, s14, 0
	v_mbcnt_hi_u32_b32 v2, s15, v2
	v_cmp_eq_u32_e32 vcc, 0, v2
	s_waitcnt vmcnt(0)
	s_and_saveexec_b64 s[30:31], vcc
	s_cbranch_execz .LBB0_321
	s_bcnt1_i32_b64 s14, s[14:15]
	v_mov_b32_e32 v2, s14
	v_readlane_b32 s14, v254, 41
	v_readlane_b32 s15, v254, 42
	s_nop 4
	global_atomic_add v195, v2, s[14:15]

.LBB0_1933:
	s_or_b64 exec, exec, s[14:15]
	v_cvt_f32_u32_e32 v6, v4
	s_waitcnt vmcnt(0)
	v_readfirstlane_b32 s9, v5
	v_sub_u32_e32 v5, 0, v4
	v_rcp_iflag_f32_e32 v6, v6
	v_add_u32_e32 v7, s9, v3
	v_mul_f32_e32 v6, 0x4f7ffffe, v6
	v_cvt_u32_f32_e32 v6, v6
	v_mul_lo_u32 v3, v5, v6
	v_mul_hi_u32 v3, v6, v3
	v_add_u32_e32 v3, v6, v3
	v_mul_hi_u32 v3, v7, v3
	v_mul_lo_u32 v5, v3, v4
	v_sub_u32_e32 v5, v7, v5
	v_add_u32_e32 v6, 1, v3
	v_cmp_ge_u32_e32 vcc, v5, v4
	s_nop 1
	v_cndmask_b32_e32 v3, v3, v6, vcc
	v_sub_u32_e32 v6, v5, v4
	v_cndmask_b32_e32 v5, v5, v6, vcc
	v_add_u32_e32 v6, 1, v3
	v_cmp_ge_u32_e32 vcc, v5, v4
	v_add_u32_e32 v5, 1, v7
	s_nop 0
	v_cndmask_b32_e32 v3, v3, v6, vcc
	v_mul_lo_u32 v6, v4, v3
	v_add_u32_e32 v4, v6, v4
	v_cmp_ne_u32_e32 vcc, v5, v4
	s_and_saveexec_b64 s[14:15], vcc
	s_xor_b64 s[30:31], exec, s[14:15]
	s_cbranch_execz .LBB0_1947
	buffer_inv sc1
	v_readlane_b32 s14, v254, 41
	v_readlane_b32 s15, v254, 42
	s_waitcnt lgkmcnt(0)
	s_nop 3
	global_load_dword v2, v195, s[14:15] sc1
	s_waitcnt vmcnt(0)
	v_cmp_eq_u32_e32 vcc, v2, v3
	s_and_saveexec_b64 s[34:35], vcc
	s_cbranch_execz .LBB0_1946
	s_mov_b32 s9, 1
	s_mov_b64 s[36:37], 0
	s_branch .LBB0_1937

.LBB0_1947:
	s_andn2_saveexec_b64 s[14:15], s[30:31]
	s_cbranch_execz .LBB0_1967
	s_mov_b64 s[14:15], exec
	buffer_wbl2 sc1
	buffer_inv sc1
	s_waitcnt lgkmcnt(0)
	s_waitcnt vmcnt(0)
	v_mbcnt_lo_u32_b32 v3, s14, 0
	v_mbcnt_hi_u32_b32 v3, s15, v3
	v_cmp_eq_u32_e32 vcc, 0, v3
	s_and_saveexec_b64 s[30:31], vcc
	s_cbranch_execz .LBB0_1950
	s_bcnt1_i32_b64 s9, s[14:15]
	v_readlane_b32 s14, v254, 43
	v_mov_b32_e32 v4, s9
	v_readlane_b32 s15, v254, 44
	s_nop 4
	global_atomic_add v4, v195, v4, s[14:15] sc0

.LBB0_1964:
	s_or_b64 exec, exec, s[14:15]
	s_mov_b64 s[14:15], exec
	v_mbcnt_lo_u32_b32 v2, s14, 0
	v_mbcnt_hi_u32_b32 v2, s15, v2
	v_cmp_eq_u32_e32 vcc, 0, v2
	s_waitcnt vmcnt(0)
	s_and_saveexec_b64 s[30:31], vcc
	s_cbranch_execz .LBB0_1966
	s_bcnt1_i32_b64 s9, s[14:15]
	v_readlane_b32 s14, v254, 41
	v_mov_b32_e32 v2, s9
	v_readlane_b32 s15, v254, 42
	s_nop 4
	global_atomic_add v195, v2, s[14:15]
